# output stores: sc1 (write-through) instead of nt
# baseline (speedup 1.0000x reference)
.LBB1_4:
	s_or_b64 exec, exec, s[4:5]
	v_lshl_or_b32 v4, v27, 1, v96
	v_lshl_or_b32 v3, v4, 7, v3
	v_or_b32_e32 v5, 0x23600, v3
	v_or_b32_e32 v3, 0x23640, v3
	s_waitcnt lgkmcnt(0)
	s_barrier
	ds_read_b32 v5, v5
	ds_read_b32 v3, v3
	v_mad_u32_u24 v4, v4, s7, v13
	v_lshl_add_u32 v4, v119, 4, v4
	v_or_b32_e32 v6, 0x20000, v4
	ds_read_b128 v[16:19], v6
	s_waitcnt lgkmcnt(1)
	v_add_f32_e32 v3, v5, v3
	v_add_u32_e32 v5, 0x20020, v4
	v_add_u32_e32 v6, 0x20040, v4
	ds_read_b128 v[112:115], v5
	ds_read_b128 v[108:111], v6
	v_add_u32_e32 v5, 0x20060, v4
	v_add_u32_e32 v6, 0x20080, v4
	v_lshlrev_b32_e32 v7, 1, v101
	ds_read_b128 v[104:107], v5
	ds_read_b128 v[96:99], v6
	v_lshrrev_b32_e32 v5, 2, v100
	v_or_b32_e32 v6, v28, v125
	v_and_b32_e32 v7, 2, v7
	v_bfe_u32 v8, v0, 1, 1
	v_and_b32_e32 v164, 8, v121
	v_bfe_i32 v9, v0, 7, 1
	v_or3_b32 v8, v8, v7, v164
	v_and_b32_e32 v0, 12, v0
	v_add_lshl_u32 v10, v6, v5, 8
	v_or_b32_e32 v5, v6, v5
	v_and_b32_e32 v9, 0xc000, v9
	v_lshlrev_b32_e32 v12, 8, v5
	v_bitop3_b32 v5, v0, v8, v124 bitop3:0x36
	v_lshl_or_b32 v13, v5, 4, v9
	v_bitop3_b32 v6, v0, v8, v2 bitop3:0x36
	v_or_b32_e32 v15, 0x1000, v12
	v_lshl_or_b32 v14, v6, 4, v9
	v_add_u32_e32 v7, v13, v15
	v_or_b32_e32 v24, 0x1400, v12
	v_or_b32_e32 v20, v7, v1
	v_add_u32_e32 v7, v14, v24
	v_add_u32_e32 v25, 0x2000, v10
	v_add_u32_e32 v5, v13, v12
	v_add_u32_e32 v6, v14, v12
	v_or_b32_e32 v22, v7, v1
	v_add_u32_e32 v7, v13, v25
	v_add_u32_e32 v150, 0x3000, v10
	v_or_b32_e32 v8, 4, v8
	v_add_u32_e32 v4, 0x200a0, v4
	v_or_b32_e32 v5, v5, v1
	v_or_b32_e32 v6, v6, v1
	v_or_b32_e32 v27, v7, v1
	v_add_u32_e32 v31, v13, v150
	v_add_u32_e32 v151, 0x3400, v10
	v_bitop3_b32 v124, v0, v8, v124 bitop3:0x36
	v_bitop3_b32 v0, v0, v8, v2 bitop3:0x36
	ds_read_b128 v[100:103], v4
	ds_read_b64_tr_b16 v[4:5], v5
	ds_read_b64_tr_b16 v[6:7], v6 offset:1024
	ds_read_b64_tr_b16 v[20:21], v20
	ds_read_b64_tr_b16 v[22:23], v22
	ds_read_b64_tr_b16 v[28:29], v27
	v_add_u32_e32 v27, 0x2400, v10
	v_or_b32_e32 v128, v31, v1
	v_add_u32_e32 v31, v14, v151
	v_add_u32_e32 v152, 0x4000, v10
	v_add_u32_e32 v158, 0x4400, v10
	v_lshl_or_b32 v124, v124, 4, v9
	v_lshl_or_b32 v0, v0, 4, v9
	v_add_u32_e32 v11, 0x5000, v10
	v_add_u32_e32 v30, v14, v27
	v_or_b32_e32 v130, v31, v1
	v_add_u32_e32 v31, v13, v152
	v_add_u32_e32 v134, v14, v158
	v_add_u32_e32 v10, 0x5400, v10
	v_add_u32_e32 v135, v124, v12
	v_add_u32_e32 v2, v0, v12
	v_add_u32_e32 v8, v124, v15
	v_or_b32_e32 v30, v30, v1
	v_or_b32_e32 v132, v31, v1
	v_or_b32_e32 v134, v134, v1
	v_add_u32_e32 v13, v13, v11
	v_add_u32_e32 v14, v14, v10
	v_or_b32_e32 v140, v135, v1
	v_or_b32_e32 v2, v2, v1
	v_or_b32_e32 v8, v8, v1
	v_add_u32_e32 v9, v0, v24
	v_add_u32_e32 v12, v124, v25
	ds_read_b64_tr_b16 v[30:31], v30
	ds_read_b64_tr_b16 v[128:129], v128
	ds_read_b64_tr_b16 v[130:131], v130
	ds_read_b64_tr_b16 v[132:133], v132
	v_or_b32_e32 v13, v13, v1
	v_or_b32_e32 v14, v14, v1
	ds_read_b64_tr_b16 v[134:135], v134
	ds_read_b64_tr_b16 v[136:137], v13
	ds_read_b64_tr_b16 v[138:139], v14
	ds_read_b64_tr_b16 v[140:141], v140
	v_or_b32_e32 v9, v9, v1
	v_or_b32_e32 v12, v12, v1
	ds_read_b64_tr_b16 v[142:143], v2 offset:1024
	ds_read_b64_tr_b16 v[144:145], v8
	ds_read_b64_tr_b16 v[146:147], v9
	ds_read_b64_tr_b16 v[148:149], v12
	v_add_u32_e32 v2, v0, v27
	v_add_u32_e32 v8, v124, v150
	v_or_b32_e32 v2, v2, v1
	v_or_b32_e32 v8, v8, v1
	v_add_u32_e32 v9, v0, v151
	v_add_u32_e32 v12, v124, v152
	v_or_b32_e32 v9, v9, v1
	v_or_b32_e32 v12, v12, v1
	ds_read_b64_tr_b16 v[150:151], v2
	ds_read_b64_tr_b16 v[152:153], v8
	ds_read_b64_tr_b16 v[154:155], v9
	ds_read_b64_tr_b16 v[156:157], v12
	v_add_u32_e32 v2, v0, v158
	v_add_u32_e32 v8, v124, v11
	v_add_u32_e32 v0, v0, v10
	v_or_b32_e32 v2, v2, v1
	v_or_b32_e32 v8, v8, v1
	v_or_b32_e32 v0, v0, v1
	v_div_scale_f32 v1, s[8:9], v3, v3, 1.0
	v_rcp_f32_e32 v9, v1
	ds_read_b64_tr_b16 v[158:159], v2
	ds_read_b64_tr_b16 v[160:161], v8
	ds_read_b64_tr_b16 v[162:163], v0
	s_mov_b32 s4, 0xc000
	s_movk_i32 s5, 0x4000
	v_fma_f32 v0, -v1, v9, 1.0
	v_fmac_f32_e32 v9, v0, v9
	v_div_scale_f32 v0, vcc, 1.0, v3, 1.0
	v_mul_f32_e32 v2, v0, v9
	v_fma_f32 v8, -v1, v2, v0
	v_fmac_f32_e32 v2, v8, v9
	v_fma_f32 v0, -v1, v2, v0
	v_div_fmas_f32 v0, v0, v9, v2
	v_div_fixup_f32 v124, v0, v3, 1.0
	s_waitcnt lgkmcnt(14)
	v_mfma_f32_32x32x16_f16 v[0:15], v[4:7], v[16:19], 0
	s_mov_b32 s7, 0x18000
	v_lshlrev_b32_e32 v172, 2, v126
	v_mov_b32_e32 v173, 0
	v_mfma_f32_32x32x16_f16 v[0:15], v[20:23], v[112:115], v[0:15]
	v_or_b32_e32 v20, v26, v116
	v_and_b32_e32 v21, 0x4000, v118
	v_lshl_or_b32 v20, v20, 8, v21
	v_bitop3_b32 v118, v121, v120, 8 bitop3:0x6c
	v_or3_b32 v121, v20, v125, s7
	v_mfma_f32_32x32x16_f16 v[0:15], v[28:31], v[108:111], v[0:15]
	v_mfma_f32_32x32x16_f16 v[0:15], v[128:131], v[104:107], v[0:15]
	v_mfma_f32_32x32x16_f16 v[0:15], v[132:135], v[96:99], v[0:15]
	s_waitcnt lgkmcnt(12)
	v_mfma_f32_32x32x16_f16 v[0:15], v[136:139], v[100:103], v[0:15]
	s_nop 11
	v_fma_mixlo_f16 v20, v124, v0, 0
	v_mov_b32_e32 v0, v1
	v_mov_b32_e32 v1, v2
	v_pk_mul_f32 v[0:1], v[124:125], v[0:1] op_sel_hi:[0,1]
	v_cvt_pk_f16_f32 v1, v0, v1
	v_pack_b32_f16 v0, v20, v1
	s_waitcnt lgkmcnt(10)
	v_mfma_f32_32x32x16_f16 v[16:31], v[140:143], v[16:19], 0
	v_fma_mixlo_f16 v2, v124, v3, 0
	v_alignbit_b32 v1, v2, v1, 16
	v_lshl_or_b32 v2, v118, 4, v121
	ds_write_b64 v2, v[0:1]
	v_mov_b32_e32 v0, v5
	v_mov_b32_e32 v1, v6
	v_pk_mul_f32 v[0:1], v[124:125], v[0:1] op_sel_hi:[0,1]
	s_waitcnt lgkmcnt(9)
	v_mfma_f32_32x32x16_f16 v[16:31], v[144:147], v[112:115], v[16:31]
	v_fma_mixlo_f16 v2, v124, v4, 0
	v_cvt_pk_f16_f32 v1, v0, v1
	v_pack_b32_f16 v0, v2, v1
	v_fma_mixlo_f16 v2, v124, v7, 0
	v_alignbit_b32 v1, v2, v1, 16
	v_bitop3_b32 v2, v164, v120, 1 bitop3:0x36
	v_lshl_or_b32 v2, v2, 4, v121
	s_waitcnt lgkmcnt(7)
	v_mfma_f32_32x32x16_f16 v[16:31], v[148:151], v[108:111], v[16:31]
	ds_write_b64 v2, v[0:1]
	v_mov_b32_e32 v0, v9
	v_mov_b32_e32 v1, v10
	v_mul_f32_e64 v0, v124, v0
	v_mul_f32_e64 v1, v124, v1
	v_fma_mixlo_f16 v2, v124, v8, 0
	v_cvt_pk_f16_f32 v1, v0, v1
	v_pack_b32_f16 v0, v2, v1
	s_waitcnt lgkmcnt(6)
	v_mfma_f32_32x32x16_f16 v[16:31], v[152:155], v[104:107], v[16:31]
	v_fma_mixlo_f16 v2, v124, v11, 0
	v_alignbit_b32 v1, v2, v1, 16
	v_bitop3_b32 v2, v164, v120, 2 bitop3:0x36
	v_lshl_or_b32 v2, v2, 4, v121
	ds_write_b64 v2, v[0:1]
	v_mov_b32_e32 v0, v13
	v_mov_b32_e32 v1, v14
	s_waitcnt lgkmcnt(5)
	v_mfma_f32_32x32x16_f16 v[16:31], v[156:159], v[96:99], v[16:31]
	v_mul_f32_e64 v0, v124, v0
	v_mul_f32_e64 v1, v124, v1
	v_fma_mixlo_f16 v2, v124, v12, 0
	v_cvt_pk_f16_f32 v1, v0, v1
	v_pack_b32_f16 v0, v2, v1
	v_fma_mixlo_f16 v2, v124, v15, 0
	v_alignbit_b32 v1, v2, v1, 16
	v_bitop3_b32 v2, v164, v120, 3 bitop3:0x36
	s_waitcnt lgkmcnt(3)
	v_mfma_f32_32x32x16_f16 v[16:31], v[160:163], v[100:103], v[16:31]
	v_lshl_or_b32 v2, v2, 4, v121
	ds_write_b64 v2, v[0:1]
	s_nop 9
	v_mov_b32_e32 v0, v17
	v_mov_b32_e32 v1, v18
	v_pk_mul_f32 v[0:1], v[124:125], v[0:1] op_sel_hi:[0,1]
	v_fma_mixlo_f16 v2, v124, v16, 0
	v_cvt_pk_f16_f32 v1, v0, v1
	v_pack_b32_f16 v0, v2, v1
	v_fma_mixlo_f16 v2, v124, v19, 0
	v_alignbit_b32 v1, v2, v1, 16
	v_bitop3_b32 v2, v164, v120, 4 bitop3:0x36
	v_lshl_or_b32 v2, v2, 4, v121
	ds_write_b64 v2, v[0:1]
	v_mov_b32_e32 v0, v21
	v_mov_b32_e32 v1, v22
	v_pk_mul_f32 v[0:1], v[124:125], v[0:1] op_sel_hi:[0,1]
	v_fma_mixlo_f16 v2, v124, v20, 0
	v_cvt_pk_f16_f32 v1, v0, v1
	v_pack_b32_f16 v0, v2, v1
	v_fma_mixlo_f16 v2, v124, v23, 0
	v_alignbit_b32 v1, v2, v1, 16
	v_bitop3_b32 v2, v164, v120, 5 bitop3:0x36
	v_lshl_or_b32 v2, v2, 4, v121
	ds_write_b64 v2, v[0:1]
	v_mov_b32_e32 v0, v25
	v_mov_b32_e32 v1, v26
	v_pk_mul_f32 v[0:1], v[124:125], v[0:1] op_sel_hi:[0,1]
	v_fma_mixlo_f16 v2, v124, v24, 0
	v_cvt_pk_f16_f32 v1, v0, v1
	v_pack_b32_f16 v0, v2, v1
	v_fma_mixlo_f16 v2, v124, v27, 0
	v_alignbit_b32 v1, v2, v1, 16
	v_bitop3_b32 v2, v164, v120, 6 bitop3:0x36
	v_lshl_or_b32 v2, v2, 4, v121
	ds_write_b64 v2, v[0:1]
	v_mov_b32_e32 v0, v29
	v_mov_b32_e32 v1, v30
	v_pk_mul_f32 v[0:1], v[124:125], v[0:1] op_sel_hi:[0,1]
	v_fma_mixlo_f16 v2, v124, v28, 0
	v_cvt_pk_f16_f32 v1, v0, v1
	v_pack_b32_f16 v0, v2, v1
	v_fma_mixlo_f16 v2, v124, v31, 0
	v_alignbit_b32 v1, v2, v1, 16
	v_bitop3_b32 v2, v164, v120, 7 bitop3:0x36
	v_lshl_or_b32 v2, v2, 4, v121
	ds_write_b64 v2, v[0:1]
	v_lshl_add_u64 v[0:1], s[0:1], 0, v[172:173]
	v_lshlrev_b32_e32 v172, 2, v127
	v_lshl_add_u64 v[0:1], v[0:1], 0, v[172:173]
	s_waitcnt lgkmcnt(0)
	s_barrier
	global_load_dwordx4 v[108:111], v[0:1], off
	global_load_dwordx4 v[104:107], v[0:1], off offset:32
	global_load_dwordx4 v[100:103], v[0:1], off offset:64
	global_load_dwordx4 v[96:99], v[0:1], off offset:96
	v_xor_b32_e32 v0, v119, v120
	v_bitop3_b32 v8, v119, v120, 2 bitop3:0x36
	v_lshlrev_b32_e32 v172, 4, v0
	v_lshlrev_b32_e32 v174, 4, v8
	v_add_u32_e32 v0, v117, v172
	v_add_u32_e32 v8, v117, v174
	v_or_b32_e32 v1, 0x18000, v0
	v_add_u32_e32 v4, 0x1a000, v0
	v_or_b32_e32 v9, 0x18000, v8
	v_add_u32_e32 v8, 0x1a000, v8
	ds_read_b128 v[0:3], v1
	ds_read_b128 v[4:7], v4
	ds_read_b128 v[112:115], v9
	ds_read_b128 v[128:131], v8
	v_bitop3_b32 v8, v119, v120, 4 bitop3:0x36
	v_lshlrev_b32_e32 v175, 4, v8
	v_add_u32_e32 v8, v117, v175
	v_or_b32_e32 v9, 0x18000, v8
	v_add_u32_e32 v8, 0x1a000, v8
	ds_read_b128 v[132:135], v9
	ds_read_b128 v[136:139], v8
	v_bitop3_b32 v8, v119, v120, 6 bitop3:0x36
	v_lshlrev_b32_e32 v176, 4, v8
	v_add_u32_e32 v8, v117, v176
	v_or_b32_e32 v9, 0x18000, v8
	v_add_u32_e32 v8, 0x1a000, v8
	ds_read_b128 v[140:143], v9
	ds_read_b128 v[144:147], v8
	v_bitop3_b32 v8, v119, v120, 8 bitop3:0x36
	v_lshlrev_b32_e32 v177, 4, v8
	v_add_u32_e32 v8, v122, v177
	v_add_u32_e32 v9, v123, v177
	ds_read_b128 v[148:151], v8
	ds_read_b128 v[152:155], v9
	v_bitop3_b32 v8, v119, v120, 10 bitop3:0x36
	v_lshlrev_b32_e32 v178, 4, v8
	v_add_u32_e32 v8, v122, v178
	v_add_u32_e32 v9, v123, v178
	ds_read_b128 v[156:159], v8
	ds_read_b128 v[160:163], v9
	v_bitop3_b32 v8, v119, v120, 12 bitop3:0x36
	v_lshlrev_b32_e32 v179, 4, v8
	v_add_u32_e32 v8, v122, v179
	v_add_u32_e32 v9, v123, v179
	ds_read_b128 v[164:167], v8
	ds_read_b128 v[168:171], v9
	v_bitop3_b32 v8, v119, v120, 14 bitop3:0x36
	v_lshlrev_b32_e32 v180, 4, v8
	v_add_u32_e32 v8, v122, v180
	v_add_u32_e32 v9, v123, v180
	ds_read_b128 v[118:121], v8
	ds_read_b128 v[122:125], v9
	s_waitcnt vmcnt(19) lgkmcnt(14)
	v_mfma_f32_32x32x16_f16 v[16:31], v[36:39], v[0:3], 0
	v_mfma_f32_32x32x16_f16 v[0:15], v[36:39], v[4:7], 0
	s_waitcnt vmcnt(18) lgkmcnt(13)
	v_mfma_f32_32x32x16_f16 v[16:31], v[32:35], v[112:115], v[16:31]
	s_waitcnt lgkmcnt(12)
	v_mfma_f32_32x32x16_f16 v[0:15], v[32:35], v[128:131], v[0:15]
	s_waitcnt vmcnt(17) lgkmcnt(11)
	v_mfma_f32_32x32x16_f16 v[16:31], v[64:67], v[132:135], v[16:31]
	s_waitcnt lgkmcnt(10)
	v_mfma_f32_32x32x16_f16 v[0:15], v[64:67], v[136:139], v[0:15]
	s_waitcnt vmcnt(16) lgkmcnt(9)
	v_mfma_f32_32x32x16_f16 v[16:31], v[48:51], v[140:143], v[16:31]
	s_waitcnt lgkmcnt(8)
	v_mfma_f32_32x32x16_f16 v[0:15], v[48:51], v[144:147], v[0:15]
	v_or_b32_e32 v140, 0x1c000, v117
	v_or_b32_e32 v117, 0x1e000, v117
	v_add_u32_e32 v32, v140, v172
	v_add_u32_e32 v36, v117, v172
	v_add_u32_e32 v48, v140, v174
	v_add_u32_e32 v64, v117, v174
	v_add_u32_e32 v112, v140, v175
	v_add_u32_e32 v128, v117, v175
	v_add_u32_e32 v132, v140, v176
	v_add_u32_e32 v136, v117, v176
	ds_read_b128 v[32:35], v32
	ds_read_b128 v[36:39], v36
	ds_read_b128 v[48:51], v48
	ds_read_b128 v[64:67], v64
	ds_read_b128 v[112:115], v112
	ds_read_b128 v[128:131], v128
	ds_read_b128 v[132:135], v132
	ds_read_b128 v[136:139], v136
	s_waitcnt vmcnt(13) lgkmcnt(14)
	v_mfma_f32_32x32x16_f16 v[16:31], v[92:95], v[148:151], v[16:31]
	v_mfma_f32_32x32x16_f16 v[0:15], v[92:95], v[152:155], v[0:15]
	s_waitcnt lgkmcnt(13)
	v_mfma_f32_32x32x16_f16 v[16:31], v[84:87], v[156:159], v[16:31]
	s_waitcnt lgkmcnt(12)
	v_mfma_f32_32x32x16_f16 v[0:15], v[84:87], v[160:163], v[0:15]
	s_waitcnt lgkmcnt(11)
	v_mfma_f32_32x32x16_f16 v[16:31], v[80:83], v[164:167], v[16:31]
	s_waitcnt lgkmcnt(10)
	v_mfma_f32_32x32x16_f16 v[0:15], v[80:83], v[168:171], v[0:15]
	s_waitcnt vmcnt(8) lgkmcnt(9)
	v_mfma_f32_32x32x16_f16 v[16:31], v[88:91], v[118:121], v[16:31]
	s_waitcnt lgkmcnt(8)
	v_mfma_f32_32x32x16_f16 v[0:15], v[88:91], v[122:125], v[0:15]
	v_add_u32_e32 v80, v140, v177
	v_add_u32_e32 v84, v117, v177
	v_add_u32_e32 v88, v140, v178
	v_add_u32_e32 v92, v117, v178
	v_add_u32_e32 v118, v140, v179
	v_add_u32_e32 v122, v117, v179
	v_add_u32_e32 v140, v140, v180
	ds_read_b128 v[80:83], v80
	ds_read_b128 v[84:87], v84
	ds_read_b128 v[88:91], v88
	ds_read_b128 v[92:95], v92
	ds_read_b128 v[118:121], v118
	ds_read_b128 v[122:125], v122
	v_add_u32_e32 v117, v117, v180
	ds_read_b128 v[140:143], v140
	ds_read_b128 v[144:147], v117
	s_waitcnt lgkmcnt(14)
	v_mfma_f32_32x32x16_f16 v[16:31], v[76:79], v[32:35], v[16:31]
	v_mfma_f32_32x32x16_f16 v[0:15], v[76:79], v[36:39], v[0:15]
	s_waitcnt lgkmcnt(13)
	v_mfma_f32_32x32x16_f16 v[16:31], v[72:75], v[48:51], v[16:31]
	s_waitcnt lgkmcnt(12)
	v_mfma_f32_32x32x16_f16 v[0:15], v[72:75], v[64:67], v[0:15]
	s_waitcnt lgkmcnt(11)
	v_mfma_f32_32x32x16_f16 v[16:31], v[68:71], v[112:115], v[16:31]
	s_waitcnt lgkmcnt(10)
	v_mfma_f32_32x32x16_f16 v[0:15], v[68:71], v[128:131], v[0:15]
	s_waitcnt lgkmcnt(9)
	v_mfma_f32_32x32x16_f16 v[16:31], v[52:55], v[132:135], v[16:31]
	s_waitcnt lgkmcnt(8)
	v_mfma_f32_32x32x16_f16 v[0:15], v[52:55], v[136:139], v[0:15]
	s_waitcnt vmcnt(7) lgkmcnt(7)
	v_mfma_f32_32x32x16_f16 v[16:31], v[60:63], v[80:83], v[16:31]
	s_waitcnt lgkmcnt(6)
	v_mfma_f32_32x32x16_f16 v[0:15], v[60:63], v[84:87], v[0:15]
	s_waitcnt vmcnt(6) lgkmcnt(5)
	v_mfma_f32_32x32x16_f16 v[16:31], v[56:59], v[88:91], v[16:31]
	s_waitcnt lgkmcnt(4)
	v_mfma_f32_32x32x16_f16 v[0:15], v[56:59], v[92:95], v[0:15]
	s_waitcnt vmcnt(5) lgkmcnt(3)
	v_mfma_f32_32x32x16_f16 v[16:31], v[44:47], v[118:121], v[16:31]
	s_waitcnt lgkmcnt(2)
	v_mfma_f32_32x32x16_f16 v[0:15], v[44:47], v[122:125], v[0:15]
	s_waitcnt vmcnt(4) lgkmcnt(1)
	v_mfma_f32_32x32x16_f16 v[16:31], v[40:43], v[140:143], v[16:31]
	s_waitcnt lgkmcnt(0)
	v_mfma_f32_32x32x16_f16 v[0:15], v[40:43], v[144:147], v[0:15]
	s_lshl_b64 s[0:1], s[2:3], 22
	s_add_u32 s0, s12, s0
	v_or_b32_e32 v32, s14, v116
	s_addc_u32 s1, s13, s1
	v_lshlrev_b32_e32 v172, 3, v32
	v_or_b32_e32 v36, v126, v127
	v_lshl_add_u64 v[32:33], s[0:1], 0, v[172:173]
	v_lshlrev_b32_e32 v172, 14, v36
	v_lshl_add_u64 v[32:33], v[32:33], 0, v[172:173]
	s_nop 0
	v_mov_b32_e32 v34, v16
	s_nop 0
	v_mov_b32_e32 v35, v0
	v_mov_b32_e32 v0, v17
	v_add_co_u32_e32 v16, vcc, s5, v32
	s_waitcnt vmcnt(3)
	v_pk_add_f32 v[0:1], v[108:109], v[0:1] op_sel:[1,0]
	v_addc_co_u32_e32 v17, vcc, 0, v33, vcc
	s_mov_b32 s0, 0x8000
	global_store_dwordx2 v[16:17], v[0:1], off sc1
	v_mov_b32_e32 v0, v18
	v_mov_b32_e32 v1, v2
	v_add_co_u32_e32 v16, vcc, s0, v32
	v_pk_add_f32 v[0:1], v[110:111], v[0:1] op_sel_hi:[0,1]
	s_nop 0
	v_addc_co_u32_e32 v17, vcc, 0, v33, vcc
	global_store_dwordx2 v[16:17], v[0:1], off sc1
	v_mov_b32_e32 v0, v111
	v_mov_b32_e32 v2, v19
	v_pk_add_f32 v[0:1], v[0:1], v[2:3] op_sel_hi:[0,1]
	v_add_co_u32_e32 v2, vcc, s4, v32
	s_mov_b32 s0, 0x24000
	s_nop 0
	v_addc_co_u32_e32 v3, vcc, 0, v33, vcc
	global_store_dwordx2 v[2:3], v[0:1], off sc1
	v_mov_b32_e32 v0, v20
	v_mov_b32_e32 v1, v4
	v_add_co_u32_e32 v2, vcc, s6, v32
	s_waitcnt vmcnt(5)
	v_pk_add_f32 v[0:1], v[104:105], v[0:1] op_sel_hi:[0,1]
	v_addc_co_u32_e32 v3, vcc, 0, v33, vcc
	global_store_dwordx2 v[2:3], v[0:1], off sc1
	v_mov_b32_e32 v4, v21
	v_add_co_u32_e32 v2, vcc, s0, v32
	v_pk_add_f32 v[0:1], v[104:105], v[4:5] op_sel:[1,0]
	s_nop 0
	v_addc_co_u32_e32 v3, vcc, 0, v33, vcc
	s_mov_b32 s0, 0x28000
	global_store_dwordx2 v[2:3], v[0:1], off sc1
	v_mov_b32_e32 v0, v22
	v_mov_b32_e32 v1, v6
	v_add_co_u32_e32 v2, vcc, s0, v32
	v_pk_add_f32 v[0:1], v[106:107], v[0:1] op_sel_hi:[0,1]
	s_nop 0
	v_addc_co_u32_e32 v3, vcc, 0, v33, vcc
	s_mov_b32 s0, 0x2c000
	global_store_dwordx2 v[2:3], v[0:1], off sc1
	v_mov_b32_e32 v0, v107
	v_mov_b32_e32 v6, v23
	v_add_co_u32_e32 v2, vcc, s0, v32
	v_pk_add_f32 v[0:1], v[0:1], v[6:7] op_sel_hi:[0,1]
	s_nop 0
	v_addc_co_u32_e32 v3, vcc, 0, v33, vcc
	s_mov_b32 s0, 0x40000
	global_store_dwordx2 v[2:3], v[0:1], off sc1
	v_mov_b32_e32 v0, v24
	v_mov_b32_e32 v1, v8
	v_add_co_u32_e32 v2, vcc, s0, v32
	s_waitcnt vmcnt(8)
	v_pk_add_f32 v[0:1], v[100:101], v[0:1] op_sel_hi:[0,1]
	v_addc_co_u32_e32 v3, vcc, 0, v33, vcc
	s_mov_b32 s0, 0x44000
	global_store_dwordx2 v[2:3], v[0:1], off sc1
	v_mov_b32_e32 v8, v25
	v_add_co_u32_e32 v2, vcc, s0, v32
	v_pk_add_f32 v[0:1], v[100:101], v[8:9] op_sel:[1,0]
	s_nop 0
	v_addc_co_u32_e32 v3, vcc, 0, v33, vcc
	s_mov_b32 s0, 0x48000
	global_store_dwordx2 v[2:3], v[0:1], off sc1
	v_mov_b32_e32 v0, v26
	v_mov_b32_e32 v1, v10
	v_add_co_u32_e32 v2, vcc, s0, v32
	v_pk_add_f32 v[0:1], v[102:103], v[0:1] op_sel_hi:[0,1]
	s_nop 0
	v_addc_co_u32_e32 v3, vcc, 0, v33, vcc
	s_mov_b32 s0, 0x4c000
	global_store_dwordx2 v[2:3], v[0:1], off sc1
	v_mov_b32_e32 v0, v103
	v_mov_b32_e32 v10, v27
	v_add_co_u32_e32 v2, vcc, s0, v32
	v_pk_add_f32 v[0:1], v[0:1], v[10:11] op_sel_hi:[0,1]
	s_nop 0
	v_addc_co_u32_e32 v3, vcc, 0, v33, vcc
	s_mov_b32 s0, 0x60000
	global_store_dwordx2 v[2:3], v[0:1], off sc1
	v_mov_b32_e32 v0, v28
	v_mov_b32_e32 v1, v12
	v_add_co_u32_e32 v2, vcc, s0, v32
	s_waitcnt vmcnt(11)
	v_pk_add_f32 v[0:1], v[96:97], v[0:1] op_sel_hi:[0,1]
	v_addc_co_u32_e32 v3, vcc, 0, v33, vcc
	s_mov_b32 s0, 0x64000
	global_store_dwordx2 v[2:3], v[0:1], off sc1
	v_mov_b32_e32 v12, v29
	v_add_co_u32_e32 v2, vcc, s0, v32
	v_pk_add_f32 v[0:1], v[96:97], v[12:13] op_sel:[1,0]
	s_nop 0
	v_addc_co_u32_e32 v3, vcc, 0, v33, vcc
	s_mov_b32 s0, 0x68000
	global_store_dwordx2 v[2:3], v[0:1], off sc1
	v_mov_b32_e32 v0, v30
	v_mov_b32_e32 v1, v14
	v_add_co_u32_e32 v2, vcc, s0, v32
	v_pk_add_f32 v[0:1], v[98:99], v[0:1] op_sel_hi:[0,1]
	s_nop 0
	v_addc_co_u32_e32 v3, vcc, 0, v33, vcc
	global_store_dwordx2 v[2:3], v[0:1], off sc1
	v_mov_b32_e32 v0, v99
	v_mov_b32_e32 v14, v31
	v_add_co_u32_e32 v2, vcc, 0x6c000, v32
	v_pk_add_f32 v[34:35], v[108:109], v[34:35] op_sel_hi:[0,1]
	v_pk_add_f32 v[0:1], v[0:1], v[14:15] op_sel_hi:[0,1]
	v_addc_co_u32_e32 v3, vcc, 0, v33, vcc
	global_store_dwordx2 v[32:33], v[34:35], off sc1
	global_store_dwordx2 v[2:3], v[0:1], off sc1
	s_endpgm
